# final stack plus three small latency items: P5 combine loads in one batch, P7 LN store-drain waits relaxed, P11 idle workgroups convert 2 tiles
# speedup vs baseline: 1.0047x; 1.0047x over previous
; template <bool STEAL>
; __device__ __forceinline__ void f8_convert(const Args& a, LAS unsigned char* lds, unsigned char* ws, int l, int first, int stride, int quota, unsigned* ticket, int tid, int lane, int wave) {
;     ...
;     if constexpr (STEAL) {
;         __syncthreads();
;         if (first != -2) {
;             if (tid == 0) word[0] = (quota > 0) ? (int)__hip_atomic_fetch_add(ticket, 1u, __ATOMIC_RELAXED, __HIP_MEMORY_SCOPE_AGENT) : F8_TILES_PER_LAYER;
;             __syncthreads(); }
;         k = word[0];
; __global__ void __launch_bounds__(NTHREADS, 2) hybrid_fwd(Args a) {
;     ...
;             if (l + 1 < NLAYER && G == 256 && (xm ? ((bid & 7) * (G >> 3) + (bid >> 3)) : bid) >= tot - hiB)
;                 f8_convert<true>(a, lds, ws, l + 1, 0, 0, 1, (unsigned*)(ws + WS_CTL) + CW_TICK + 64 * (l + 1), tid, lane, wave);
.LBB0_1214:
	s_cmp_eq_u32 s66, 3
	s_cselect_b64 s[0:1], -1, 0
	s_xor_b64 s[6:7], s[96:97], -1
	s_or_b64 s[0:1], s[6:7], s[0:1]
	s_and_b64 vcc, exec, s[0:1]
	s_cbranch_vccnz .LBB0_1284
	s_lshl_b32 s0, s22, 5
	s_and_b32 s0, s0, 0xe0
	s_ashr_i32 s1, s22, 3
	s_add_i32 s6, s0, s1
	s_and_b64 s[0:1], s[2:3], exec
	s_cselect_b32 s0, s22, s6
	s_cmp_lt_i32 s0, s23
	s_cbranch_scc1 .LBB0_1284
	s_add_i32 s18, s66, 1
	s_lshl_b32 s92, s18, 6
	s_add_i32 s14, s20, 0x20640
	v_cmp_eq_u32_e64 s[0:1], 0, v161
	s_waitcnt lgkmcnt(0)
	s_barrier
	s_and_saveexec_b64 s[2:3], s[0:1]
	s_cbranch_execz .LBB0_1218
	s_lshl_b64 s[6:7], s[92:93], 2
	s_add_u32 s6, s4, s6
	s_addc_u32 s7, s5, s7
	v_mov_b32_e32 v0, s6
	v_add_co_u32_e32 v0, vcc, 0x9000, v0
	v_mov_b32_e32 v1, s7
	s_nop 0
	v_addc_co_u32_e32 v1, vcc, 0, v1, vcc
	v_mov_b32_e32 v178, v0
	v_mov_b32_e32 v179, v1
	flat_atomic_add v0, v[0:1], v206 sc0
	v_mov_b32_e32 v1, s14
	s_waitcnt vmcnt(0) lgkmcnt(0)
	ds_write_b32 v1, v0

; #define LAS __attribute__((address_space(3)))
; template <bool STEAL>
; __device__ __forceinline__ void f8_convert(const Args& a, LAS unsigned char* lds, unsigned char* ws, int l, int first, int stride, int quota, unsigned* ticket, int tid, int lane, int wave) {
;     ...
;         if constexpr (STEAL) { if (tid == 0) word[(n + 1) & 1] = (n + 1 < quota) ? (int)__hip_atomic_fetch_add(ticket, 1u, __ATOMIC_RELAXED, __HIP_MEMORY_SCOPE_AGENT) : F8_TILES_PER_LAYER; }
;         const float sc = T.scale;
; #pragma unroll
;         for (int c = 0; c < 4; ++c) {
;             const int R = T.drow + c * T.dstep, sw = (R >> 2) & 15;
;             u32x4 lo, hi;
;             lo.x = cvt4_fp8(v[0][c] * sc, v[1][c] * sc, v[2][c] * sc, v[3][c] * sc);     lo.y = cvt4_fp8(v[4][c] * sc, v[5][c] * sc, v[6][c] * sc, v[7][c] * sc);
;             lo.z = cvt4_fp8(v[8][c] * sc, v[9][c] * sc, v[10][c] * sc, v[11][c] * sc);   lo.w = cvt4_fp8(v[12][c] * sc, v[13][c] * sc, v[14][c] * sc, v[15][c] * sc);
;             hi.x = cvt4_fp8(v[16][c] * sc, v[17][c] * sc, v[18][c] * sc, v[19][c] * sc); hi.y = cvt4_fp8(v[20][c] * sc, v[21][c] * sc, v[22][c] * sc, v[23][c] * sc);
;             hi.z = cvt4_fp8(v[24][c] * sc, v[25][c] * sc, v[26][c] * sc, v[27][c] * sc); hi.w = cvt4_fp8(v[28][c] * sc, v[29][c] * sc, v[30][c] * sc, v[31][c] * sc);
;             *(LAS u32x4*)(buf + R * 256 + (((2 * wave) ^ sw) << 4)) = lo;
;             *(LAS u32x4*)(buf + R * 256 + (((2 * wave + 1) ^ sw) << 4)) = hi;
;         }
.LBB0_1253:
	s_and_b32 s8, s21, 1
	s_and_saveexec_b64 s[4:5], s[0:1]
	s_lshl_b32 s9, s8, 2
	s_add_i32 s9, s14, s9
	v_mov_b32_e32 v128, s9
	v_mov_b32_e32 v129, 0x6e0
	s_cmp_lg_u32 s21, 1
	s_cbranch_scc1 .Lq11_w
	flat_atomic_add v129, v[178:179], v206 sc0
	s_waitcnt vmcnt(0) lgkmcnt(0)
.Lq11_w:
	ds_write_b32 v128, v129
	s_or_b64 exec, exec, s[4:5]
	s_waitcnt vmcnt(0)
	v_mul_f32_e32 v128, s37, v0
	v_mul_f32_e32 v129, s37, v4
	v_med3_f32 v168, v128, s69, v208
	v_med3_f32 v129, v129, s69, v208
	v_mov_b32_e32 v128, v193
	v_cvt_pk_fp8_f32 v128, v168, v129
	v_mul_f32_e32 v130, s37, v8
	v_mul_f32_e32 v131, s37, v12
	v_med3_f32 v130, v130, s69, v208
	v_med3_f32 v131, v131, s69, v208
	v_cvt_pk_fp8_f32 v128, v130, v131 op_sel:[0,0,1]
	v_mul_f32_e32 v129, s37, v16
	v_mul_f32_e32 v130, s37, v20
	v_med3_f32 v169, v129, s69, v208
	v_med3_f32 v130, v130, s69, v208
	v_mov_b32_e32 v129, v193
	v_cvt_pk_fp8_f32 v129, v169, v130
	v_mul_f32_e32 v131, s37, v24
	v_mul_f32_e32 v168, s37, v28
	v_med3_f32 v131, v131, s69, v208
	v_med3_f32 v168, v168, s69, v208
	v_cvt_pk_fp8_f32 v129, v131, v168 op_sel:[0,0,1]
	v_mul_f32_e32 v130, s37, v32
	v_mul_f32_e32 v131, s37, v36
	v_med3_f32 v170, v130, s69, v208
	v_med3_f32 v131, v131, s69, v208
	v_mov_b32_e32 v130, v193
	v_cvt_pk_fp8_f32 v130, v170, v131
	v_mul_f32_e32 v168, s37, v40
	v_mul_f32_e32 v169, s37, v44
	v_med3_f32 v168, v168, s69, v208
	v_med3_f32 v169, v169, s69, v208
	v_cvt_pk_fp8_f32 v130, v168, v169 op_sel:[0,0,1]
	v_mul_f32_e32 v131, s37, v48
	v_mul_f32_e32 v168, s37, v52
	v_med3_f32 v171, v131, s69, v208
	v_med3_f32 v168, v168, s69, v208
	v_mov_b32_e32 v131, v193
	v_cvt_pk_fp8_f32 v131, v171, v168
	v_mul_f32_e32 v169, s37, v56
	v_mul_f32_e32 v170, s37, v60
	v_med3_f32 v169, v169, s69, v208
	v_med3_f32 v170, v170, s69, v208
	v_cvt_pk_fp8_f32 v131, v169, v170 op_sel:[0,0,1]
	v_mul_f32_e32 v168, s37, v64
	v_mul_f32_e32 v169, s37, v68
	v_med3_f32 v173, v168, s69, v208
	v_med3_f32 v169, v169, s69, v208
	v_mov_b32_e32 v168, v193
	v_cvt_pk_fp8_f32 v168, v173, v169
	v_mul_f32_e32 v170, s37, v72
	v_mul_f32_e32 v171, s37, v76
	v_med3_f32 v170, v170, s69, v208
	v_med3_f32 v171, v171, s69, v208
	v_cvt_pk_fp8_f32 v168, v170, v171 op_sel:[0,0,1]
	v_mul_f32_e32 v169, s37, v80
	v_mul_f32_e32 v170, s37, v84
	v_med3_f32 v174, v169, s69, v208
	v_med3_f32 v170, v170, s69, v208
	v_mov_b32_e32 v169, v193
	v_cvt_pk_fp8_f32 v169, v174, v170
	v_mul_f32_e32 v171, s37, v88
	v_mul_f32_e32 v173, s37, v92
	v_med3_f32 v171, v171, s69, v208
	v_med3_f32 v173, v173, s69, v208
	v_cvt_pk_fp8_f32 v169, v171, v173 op_sel:[0,0,1]
	v_mul_f32_e32 v170, s37, v96
	v_mul_f32_e32 v171, s37, v100
	v_med3_f32 v175, v170, s69, v208
	v_med3_f32 v171, v171, s69, v208
	v_mov_b32_e32 v170, v193
	v_cvt_pk_fp8_f32 v170, v175, v171
	v_mul_f32_e32 v173, s37, v104
	v_mul_f32_e32 v174, s37, v108
	v_med3_f32 v173, v173, s69, v208
	v_med3_f32 v174, v174, s69, v208
	v_cvt_pk_fp8_f32 v170, v173, v174 op_sel:[0,0,1]
	v_mul_f32_e32 v171, s37, v112
	v_mul_f32_e32 v173, s37, v116
	v_med3_f32 v176, v171, s69, v208
	v_med3_f32 v173, v173, s69, v208
	v_mov_b32_e32 v171, v193
	v_cvt_pk_fp8_f32 v171, v176, v173
	s_and_b32 s4, s35, 0x10000
	v_mul_f32_e32 v174, s37, v120
	v_mul_f32_e32 v175, s37, v124
	s_add_i32 s38, s20, s4
	v_lshrrev_b32_e32 v172, 2, v167
	v_med3_f32 v174, v174, s69, v208
	v_med3_f32 v175, v175, s69, v208
	v_cvt_pk_fp8_f32 v171, v174, v175 op_sel:[0,0,1]
	v_lshl_add_u32 v173, v167, 8, s38
	v_bitop3_b32 v174, v172, s22, 15 bitop3:0x6c
	v_lshl_add_u32 v174, v174, 4, v173
	ds_write_b128 v174, v[128:131]
	v_bitop3_b32 v128, v172, s23, 15 bitop3:0x6c
	v_lshl_add_u32 v128, v128, 4, v173
	ds_write_b128 v128, v[168:171]
	v_mul_f32_e32 v128, s37, v1
	v_mul_f32_e32 v129, s37, v5
	v_med3_f32 v168, v128, s69, v208
	v_med3_f32 v129, v129, s69, v208
	v_mov_b32_e32 v128, v193
	v_cvt_pk_fp8_f32 v128, v168, v129
	v_mul_f32_e32 v130, s37, v9
	v_mul_f32_e32 v131, s37, v13
	v_med3_f32 v130, v130, s69, v208
	v_med3_f32 v131, v131, s69, v208
	v_cvt_pk_fp8_f32 v128, v130, v131 op_sel:[0,0,1]
	v_mul_f32_e32 v129, s37, v17
	v_mul_f32_e32 v130, s37, v21
	v_med3_f32 v169, v129, s69, v208
	v_med3_f32 v130, v130, s69, v208
	v_mov_b32_e32 v129, v193
	v_cvt_pk_fp8_f32 v129, v169, v130
	v_mul_f32_e32 v131, s37, v25
	v_mul_f32_e32 v168, s37, v29
	v_med3_f32 v131, v131, s69, v208
	v_med3_f32 v168, v168, s69, v208
	v_cvt_pk_fp8_f32 v129, v131, v168 op_sel:[0,0,1]
	v_mul_f32_e32 v130, s37, v33
	v_mul_f32_e32 v131, s37, v37
	v_med3_f32 v170, v130, s69, v208
	v_med3_f32 v131, v131, s69, v208
	v_mov_b32_e32 v130, v193
	v_cvt_pk_fp8_f32 v130, v170, v131
	v_mul_f32_e32 v168, s37, v41
	v_mul_f32_e32 v169, s37, v45
	v_med3_f32 v168, v168, s69, v208
	v_med3_f32 v169, v169, s69, v208
	v_cvt_pk_fp8_f32 v130, v168, v169 op_sel:[0,0,1]
	v_mul_f32_e32 v131, s37, v49
	v_mul_f32_e32 v168, s37, v53
	v_med3_f32 v171, v131, s69, v208
	v_med3_f32 v168, v168, s69, v208
	v_mov_b32_e32 v131, v193
	v_cvt_pk_fp8_f32 v131, v171, v168
	v_mul_f32_e32 v169, s37, v57
	v_mul_f32_e32 v170, s37, v61
	v_med3_f32 v169, v169, s69, v208
	v_med3_f32 v170, v170, s69, v208
	v_cvt_pk_fp8_f32 v131, v169, v170 op_sel:[0,0,1]
	v_mul_f32_e32 v168, s37, v65
	v_mul_f32_e32 v169, s37, v69
	v_med3_f32 v174, v168, s69, v208
	v_med3_f32 v169, v169, s69, v208
	v_mov_b32_e32 v168, v193
	v_cvt_pk_fp8_f32 v168, v174, v169
	v_mul_f32_e32 v170, s37, v73
	v_mul_f32_e32 v171, s37, v77
	v_med3_f32 v170, v170, s69, v208
	v_med3_f32 v171, v171, s69, v208
	v_cvt_pk_fp8_f32 v168, v170, v171 op_sel:[0,0,1]
	v_mul_f32_e32 v169, s37, v81
	v_mul_f32_e32 v170, s37, v85
	v_med3_f32 v175, v169, s69, v208
	v_med3_f32 v170, v170, s69, v208
	v_mov_b32_e32 v169, v193
; #define LAS __attribute__((address_space(3)))
; template <bool STEAL>
; __device__ __forceinline__ void f8_convert(const Args& a, LAS unsigned char* lds, unsigned char* ws, int l, int first, int stride, int quota, unsigned* ticket, int tid, int lane, int wave) {
;     ...
;             const int R = T.drow + c * T.dstep, sw = (R >> 2) & 15;
;             u32x4 lo, hi;
;             lo.x = cvt4_fp8(v[0][c] * sc, v[1][c] * sc, v[2][c] * sc, v[3][c] * sc);     lo.y = cvt4_fp8(v[4][c] * sc, v[5][c] * sc, v[6][c] * sc, v[7][c] * sc);
;             lo.z = cvt4_fp8(v[8][c] * sc, v[9][c] * sc, v[10][c] * sc, v[11][c] * sc);   lo.w = cvt4_fp8(v[12][c] * sc, v[13][c] * sc, v[14][c] * sc, v[15][c] * sc);
;             hi.x = cvt4_fp8(v[16][c] * sc, v[17][c] * sc, v[18][c] * sc, v[19][c] * sc); hi.y = cvt4_fp8(v[20][c] * sc, v[21][c] * sc, v[22][c] * sc, v[23][c] * sc);
;             hi.z = cvt4_fp8(v[24][c] * sc, v[25][c] * sc, v[26][c] * sc, v[27][c] * sc); hi.w = cvt4_fp8(v[28][c] * sc, v[29][c] * sc, v[30][c] * sc, v[31][c] * sc);
;             *(LAS u32x4*)(buf + R * 256 + (((2 * wave) ^ sw) << 4)) = lo;
;             *(LAS u32x4*)(buf + R * 256 + (((2 * wave + 1) ^ sw) << 4)) = hi;
;         }
	v_cvt_pk_fp8_f32 v169, v175, v170
	v_mul_f32_e32 v171, s37, v89
	v_mul_f32_e32 v174, s37, v93
	v_med3_f32 v171, v171, s69, v208
	v_med3_f32 v174, v174, s69, v208
	v_cvt_pk_fp8_f32 v169, v171, v174 op_sel:[0,0,1]
	v_mul_f32_e32 v170, s37, v97
	v_mul_f32_e32 v171, s37, v101
	v_med3_f32 v176, v170, s69, v208
	v_med3_f32 v171, v171, s69, v208
	v_mov_b32_e32 v170, v193
	v_cvt_pk_fp8_f32 v170, v176, v171
	v_mul_f32_e32 v174, s37, v105
	v_mul_f32_e32 v175, s37, v109
	v_med3_f32 v174, v174, s69, v208
	v_med3_f32 v175, v175, s69, v208
	v_cvt_pk_fp8_f32 v170, v174, v175 op_sel:[0,0,1]
	v_mul_f32_e32 v171, s37, v113
	v_mul_f32_e32 v174, s37, v117
	v_med3_f32 v177, v171, s69, v208
	v_med3_f32 v174, v174, s69, v208
	v_mov_b32_e32 v171, v193
	v_cvt_pk_fp8_f32 v171, v177, v174
	v_add_u32_e32 v172, s36, v167
	v_mul_f32_e32 v175, s37, v121
	v_mul_f32_e32 v176, s37, v125
	v_lshrrev_b32_e32 v173, 2, v172
	v_med3_f32 v175, v175, s69, v208
	v_med3_f32 v176, v176, s69, v208
	v_cvt_pk_fp8_f32 v171, v175, v176 op_sel:[0,0,1]
	v_lshl_add_u32 v174, v172, 8, s38
	v_bitop3_b32 v175, v173, s22, 15 bitop3:0x6c
	v_lshl_add_u32 v175, v175, 4, v174
	ds_write_b128 v175, v[128:131]
	v_bitop3_b32 v128, v173, s23, 15 bitop3:0x6c
	v_lshl_add_u32 v128, v128, 4, v174
	ds_write_b128 v128, v[168:171]
	v_mul_f32_e32 v128, s37, v2
	v_mul_f32_e32 v129, s37, v6
	v_med3_f32 v168, v128, s69, v208
	v_med3_f32 v129, v129, s69, v208
	v_mov_b32_e32 v128, v193
	v_cvt_pk_fp8_f32 v128, v168, v129
	v_mul_f32_e32 v130, s37, v10
	v_mul_f32_e32 v131, s37, v14
	v_med3_f32 v130, v130, s69, v208
	v_med3_f32 v131, v131, s69, v208
	v_cvt_pk_fp8_f32 v128, v130, v131 op_sel:[0,0,1]
	v_mul_f32_e32 v129, s37, v18
	v_mul_f32_e32 v130, s37, v22
	v_med3_f32 v169, v129, s69, v208
	v_med3_f32 v130, v130, s69, v208
	v_mov_b32_e32 v129, v193
	v_cvt_pk_fp8_f32 v129, v169, v130
	v_mul_f32_e32 v131, s37, v26
	v_mul_f32_e32 v168, s37, v30
	v_med3_f32 v131, v131, s69, v208
	v_med3_f32 v168, v168, s69, v208
	v_cvt_pk_fp8_f32 v129, v131, v168 op_sel:[0,0,1]
	v_mul_f32_e32 v130, s37, v34
	v_mul_f32_e32 v131, s37, v38
	v_med3_f32 v170, v130, s69, v208
	v_med3_f32 v131, v131, s69, v208
	v_mov_b32_e32 v130, v193
	v_cvt_pk_fp8_f32 v130, v170, v131
	v_mul_f32_e32 v168, s37, v42
	v_mul_f32_e32 v169, s37, v46
	v_med3_f32 v168, v168, s69, v208
	v_med3_f32 v169, v169, s69, v208
	v_cvt_pk_fp8_f32 v130, v168, v169 op_sel:[0,0,1]
	v_mul_f32_e32 v131, s37, v50
	v_mul_f32_e32 v168, s37, v54
	v_med3_f32 v171, v131, s69, v208
	v_med3_f32 v168, v168, s69, v208
	v_mov_b32_e32 v131, v193
	v_cvt_pk_fp8_f32 v131, v171, v168
	v_mul_f32_e32 v169, s37, v58
	v_mul_f32_e32 v170, s37, v62
	v_med3_f32 v169, v169, s69, v208
	v_med3_f32 v170, v170, s69, v208
	v_cvt_pk_fp8_f32 v131, v169, v170 op_sel:[0,0,1]
	v_mul_f32_e32 v168, s37, v66
	v_mul_f32_e32 v169, s37, v70
	v_med3_f32 v174, v168, s69, v208
	v_med3_f32 v169, v169, s69, v208
	v_mov_b32_e32 v168, v193
	v_cvt_pk_fp8_f32 v168, v174, v169
	v_mul_f32_e32 v170, s37, v74
	v_mul_f32_e32 v171, s37, v78
	v_med3_f32 v170, v170, s69, v208
	v_med3_f32 v171, v171, s69, v208
	v_cvt_pk_fp8_f32 v168, v170, v171 op_sel:[0,0,1]
	v_mul_f32_e32 v169, s37, v82
	v_mul_f32_e32 v170, s37, v86
	v_med3_f32 v175, v169, s69, v208
	v_med3_f32 v170, v170, s69, v208
	v_mov_b32_e32 v169, v193
	v_cvt_pk_fp8_f32 v169, v175, v170
	v_mul_f32_e32 v171, s37, v90
	v_mul_f32_e32 v174, s37, v94
	v_med3_f32 v171, v171, s69, v208
	v_med3_f32 v174, v174, s69, v208
	v_cvt_pk_fp8_f32 v169, v171, v174 op_sel:[0,0,1]
	v_mul_f32_e32 v170, s37, v98
	v_mul_f32_e32 v171, s37, v102
	v_med3_f32 v176, v170, s69, v208
	v_med3_f32 v171, v171, s69, v208
	v_mov_b32_e32 v170, v193
	v_cvt_pk_fp8_f32 v170, v176, v171
	v_mul_f32_e32 v174, s37, v106
	v_mul_f32_e32 v175, s37, v110
	v_med3_f32 v174, v174, s69, v208
	v_med3_f32 v175, v175, s69, v208
	v_cvt_pk_fp8_f32 v170, v174, v175 op_sel:[0,0,1]
	v_mul_f32_e32 v171, s37, v114
	v_mul_f32_e32 v174, s37, v118
	v_med3_f32 v177, v171, s69, v208
	v_med3_f32 v174, v174, s69, v208
	v_mov_b32_e32 v171, v193
	v_cvt_pk_fp8_f32 v171, v177, v174
	v_add_u32_e32 v172, s36, v172
	v_mul_f32_e32 v175, s37, v122
	v_mul_f32_e32 v176, s37, v126
	v_lshrrev_b32_e32 v173, 2, v172
	v_med3_f32 v175, v175, s69, v208
; #define LAS __attribute__((address_space(3)))
; #define F8_LOADS() do { _Pragma("unroll") for (int q = 0; q < 32; ++q) v[q] = __builtin_nontemporal_load((const f32x4*)(T.src + (size_t)q * T.ld)); } while (0)
; template <bool STEAL>
; __device__ __forceinline__ void f8_convert(const Args& a, LAS unsigned char* lds, unsigned char* ws, int l, int first, int stride, int quota, unsigned* ticket, int tid, int lane, int wave) {
;     ...
;             const int R = T.drow + c * T.dstep, sw = (R >> 2) & 15;
;             u32x4 lo, hi;
;             lo.x = cvt4_fp8(v[0][c] * sc, v[1][c] * sc, v[2][c] * sc, v[3][c] * sc);     lo.y = cvt4_fp8(v[4][c] * sc, v[5][c] * sc, v[6][c] * sc, v[7][c] * sc);
;             lo.z = cvt4_fp8(v[8][c] * sc, v[9][c] * sc, v[10][c] * sc, v[11][c] * sc);   lo.w = cvt4_fp8(v[12][c] * sc, v[13][c] * sc, v[14][c] * sc, v[15][c] * sc);
;             hi.x = cvt4_fp8(v[16][c] * sc, v[17][c] * sc, v[18][c] * sc, v[19][c] * sc); hi.y = cvt4_fp8(v[20][c] * sc, v[21][c] * sc, v[22][c] * sc, v[23][c] * sc);
;             hi.z = cvt4_fp8(v[24][c] * sc, v[25][c] * sc, v[26][c] * sc, v[27][c] * sc); hi.w = cvt4_fp8(v[28][c] * sc, v[29][c] * sc, v[30][c] * sc, v[31][c] * sc);
;             *(LAS u32x4*)(buf + R * 256 + (((2 * wave) ^ sw) << 4)) = lo;
;             *(LAS u32x4*)(buf + R * 256 + (((2 * wave + 1) ^ sw) << 4)) = hi;
;         }
;         __syncthreads();
;         unsigned char* const dst = T.dst; const int dpitch = T.dpitch;
;         int kn; if constexpr (STEAL) kn = word[(n + 1) & 1]; else kn = k + stride;
;         if (kn < F8_TILES_PER_LAYER) { T = f8_tile(a, lds, ws, f8_tile_of(l, kn), lane, wave); F8_LOADS(); }
	v_med3_f32 v176, v176, s69, v208
	v_cvt_pk_fp8_f32 v171, v175, v176 op_sel:[0,0,1]
	v_lshl_add_u32 v174, v172, 8, s38
	v_bitop3_b32 v175, v173, s22, 15 bitop3:0x6c
	v_lshl_add_u32 v175, v175, 4, v174
	ds_write_b128 v175, v[128:131]
	v_bitop3_b32 v128, v173, s23, 15 bitop3:0x6c
	v_lshl_add_u32 v128, v128, 4, v174
	ds_write_b128 v128, v[168:171]
	v_mul_f32_e32 v128, s37, v3
	v_mul_f32_e32 v129, s37, v7
	v_med3_f32 v168, v128, s69, v208
	v_med3_f32 v129, v129, s69, v208
	v_mov_b32_e32 v128, v193
	v_cvt_pk_fp8_f32 v128, v168, v129
	v_mul_f32_e32 v130, s37, v11
	v_mul_f32_e32 v131, s37, v15
	v_med3_f32 v130, v130, s69, v208
	v_med3_f32 v131, v131, s69, v208
	v_cvt_pk_fp8_f32 v128, v130, v131 op_sel:[0,0,1]
	v_mul_f32_e32 v129, s37, v19
	v_mul_f32_e32 v130, s37, v23
	v_med3_f32 v169, v129, s69, v208
	v_med3_f32 v130, v130, s69, v208
	v_mov_b32_e32 v129, v193
	v_cvt_pk_fp8_f32 v129, v169, v130
	v_mul_f32_e32 v131, s37, v27
	v_mul_f32_e32 v168, s37, v31
	v_med3_f32 v131, v131, s69, v208
	v_med3_f32 v168, v168, s69, v208
	v_cvt_pk_fp8_f32 v129, v131, v168 op_sel:[0,0,1]
	v_mul_f32_e32 v130, s37, v35
	v_mul_f32_e32 v131, s37, v39
	v_med3_f32 v170, v130, s69, v208
	v_med3_f32 v131, v131, s69, v208
	v_mov_b32_e32 v130, v193
	v_cvt_pk_fp8_f32 v130, v170, v131
	v_mul_f32_e32 v168, s37, v43
	v_mul_f32_e32 v169, s37, v47
	v_med3_f32 v168, v168, s69, v208
	v_med3_f32 v169, v169, s69, v208
	v_cvt_pk_fp8_f32 v130, v168, v169 op_sel:[0,0,1]
	v_mul_f32_e32 v131, s37, v51
	v_mul_f32_e32 v168, s37, v55
	v_med3_f32 v171, v131, s69, v208
	v_med3_f32 v168, v168, s69, v208
	v_mov_b32_e32 v131, v193
	v_cvt_pk_fp8_f32 v131, v171, v168
	v_mul_f32_e32 v169, s37, v59
	v_mul_f32_e32 v170, s37, v63
	v_med3_f32 v169, v169, s69, v208
	v_med3_f32 v170, v170, s69, v208
	v_cvt_pk_fp8_f32 v131, v169, v170 op_sel:[0,0,1]
	v_mul_f32_e32 v168, s37, v67
	v_mul_f32_e32 v169, s37, v71
	v_med3_f32 v174, v168, s69, v208
	v_med3_f32 v169, v169, s69, v208
	v_mov_b32_e32 v168, v193
	v_cvt_pk_fp8_f32 v168, v174, v169
	v_mul_f32_e32 v170, s37, v75
	v_mul_f32_e32 v171, s37, v79
	v_med3_f32 v170, v170, s69, v208
	v_med3_f32 v171, v171, s69, v208
	v_cvt_pk_fp8_f32 v168, v170, v171 op_sel:[0,0,1]
	v_mul_f32_e32 v169, s37, v83
	v_mul_f32_e32 v170, s37, v87
	v_med3_f32 v175, v169, s69, v208
	v_med3_f32 v170, v170, s69, v208
	v_mov_b32_e32 v169, v193
	v_cvt_pk_fp8_f32 v169, v175, v170
	v_mul_f32_e32 v171, s37, v91
	v_mul_f32_e32 v174, s37, v95
	v_med3_f32 v171, v171, s69, v208
	v_med3_f32 v174, v174, s69, v208
	v_cvt_pk_fp8_f32 v169, v171, v174 op_sel:[0,0,1]
	v_mul_f32_e32 v170, s37, v99
	v_mul_f32_e32 v171, s37, v103
	v_med3_f32 v176, v170, s69, v208
	v_med3_f32 v171, v171, s69, v208
	v_mov_b32_e32 v170, v193
	v_cvt_pk_fp8_f32 v170, v176, v171
	v_mul_f32_e32 v174, s37, v107
	v_mul_f32_e32 v175, s37, v111
	v_med3_f32 v174, v174, s69, v208
	v_med3_f32 v175, v175, s69, v208
	v_cvt_pk_fp8_f32 v170, v174, v175 op_sel:[0,0,1]
	v_mul_f32_e32 v171, s37, v115
	v_mul_f32_e32 v174, s37, v119
	v_med3_f32 v177, v171, s69, v208
	v_med3_f32 v174, v174, s69, v208
	v_mov_b32_e32 v171, v193
	v_cvt_pk_fp8_f32 v171, v177, v174
	v_add_u32_e32 v172, s36, v172
	v_mul_f32_e32 v175, s37, v123
	v_mul_f32_e32 v176, s37, v127
	v_lshrrev_b32_e32 v173, 2, v172
	v_med3_f32 v175, v175, s69, v208
	v_med3_f32 v176, v176, s69, v208
	v_cvt_pk_fp8_f32 v171, v175, v176 op_sel:[0,0,1]
	v_lshl_add_u32 v172, v172, 8, s38
	v_bitop3_b32 v174, v173, s22, 15 bitop3:0x6c
	v_lshl_add_u32 v174, v174, 4, v172
	ds_write_b128 v174, v[128:131]
	v_bitop3_b32 v128, v173, s23, 15 bitop3:0x6c
	s_lshl_b32 s4, s8, 2
	v_lshl_add_u32 v128, v128, 4, v172
	s_add_i32 s4, s14, s4
	ds_write_b128 v128, v[168:171]
	v_mov_b32_e32 v128, s4
	s_waitcnt lgkmcnt(0)
	s_barrier
	ds_read_b32 v128, v128
	s_movk_i32 s4, 0x6df
	s_mov_b64 s[8:9], s[6:7]
	s_waitcnt lgkmcnt(0)
	v_cmp_lt_i32_e64 s[4:5], s4, v128
	v_readfirstlane_b32 s10, v128
	s_and_b64 vcc, exec, s[4:5]
	v_mov_b32_e32 v128, v151
	s_cbranch_vccnz .LBB0_1252
	s_cmpk_gt_i32 s10, 0x9f
	s_mov_b64 s[8:9], -1
	s_cbranch_scc0 .LBB0_1279
	s_cmpk_gt_u32 s10, 0x49f
	s_cbranch_scc0 .LBB0_1263
	s_cmpk_gt_u32 s10, 0x69f
	s_cbranch_scc0 .LBB0_1260
	s_add_i32 s39, s15, s10
	s_mov_b64 s[8:9], 0
